# baseline (speedup 1.0000x reference)
_Z12conv3_kernelPK15HIP_vector_typeIjLj4EES2_PKfPfS5_:
	v_min_u32_e32 v125, 0x13f, v0
	v_lshlrev_b32_e32 v125, 7, v125
	s_lshl_b32 s3, s3, 7
	s_add_i32 s3, s3, s2
	s_lshl_b32 s2, s2, 5
	s_and_b32 s2, s2, 0xe0
	s_ashr_i32 s3, s3, 3
	s_add_i32 s3, s3, s2
	s_lshl_b32 s2, s3, 8
	s_load_dwordx4 s[8:11], s[0:1], 0x0
	s_ashr_i32 s14, s3, 7
	s_and_b32 s15, s2, 0x7f00
	s_mul_i32 s2, s14, 0x40c00
	s_or_b32 s4, s15, 7
	s_mul_hi_i32 s3, s14, 0x40c00
	s_add_u32 s2, s2, s4
	s_addc_u32 s3, s3, 0
	s_lshl_b64 s[2:3], s[2:3], 6
	s_waitcnt lgkmcnt(0)
	s_add_u32 s8, s8, s2
	s_addc_u32 s9, s9, s3
	v_mov_b32_e32 v65, 0
	v_lshlrev_b32_e32 v64, 4, v0
	v_lshl_add_u64 v[2:3], s[8:9], 0, v[64:65]
	s_movk_i32 s2, 0x2000
	v_add_co_u32_e32 v4, vcc, s2, v2
	v_or_b32_e32 v1, 0x400, v0
	s_nop 0
	v_addc_co_u32_e32 v5, vcc, 0, v3, vcc
	v_add_co_u32_e32 v2, vcc, 0x6000, v2
	v_lshlrev_b32_e32 v76, 4, v1
	global_load_dwordx4 v[10:13], v[4:5], off
	global_load_dwordx4 v[6:9], v76, s[8:9]
	v_addc_co_u32_e32 v3, vcc, 0, v3, vcc
	global_load_dwordx4 v[18:21], v64, s[8:9]
	global_load_dwordx4 v[14:17], v[2:3], off
	v_or_b32_e32 v34, 0x800, v0
	s_movk_i32 s2, 0x9b8
	v_cmp_gt_u32_e64 s[2:3], s2, v34
	v_lshlrev_b32_e32 v78, 4, v34
	v_mov_b32_e32 v2, 0
	v_mov_b32_e32 v3, 0
	v_mov_b32_e32 v4, 0
	v_mov_b32_e32 v5, 0
	s_and_saveexec_b64 s[4:5], s[2:3]
	s_cbranch_execz .LBB4_2
	global_load_dwordx4 v[2:5], v78, s[8:9]

.LBB4_16:
	s_or_b64 exec, exec, s[12:13]
	s_add_u32 s16, s8, 0x40c000
	s_addc_u32 s17, s9, 0
	global_load_dword v124, v125, s[16:17]
	v_and_b32_e32 v1, 31, v0
	v_lshrrev_b32_e32 v2, 5, v0
	v_bfe_u32 v66, v0, 5, 1
	v_lshrrev_b32_e32 v3, 1, v0
	v_bfe_u32 v0, v0, 2, 2
	v_bitop3_b32 v2, v2, v0, 1 bitop3:0x6c
	s_movk_i32 s6, 0xe0
	v_lshlrev_b32_e32 v2, 4, v2
	v_lshlrev_b32_e32 v24, 6, v1
	v_and_or_b32 v67, v3, s6, v1
	v_or_b32_e32 v1, v24, v2
	v_add_u32_e32 v75, 0x13700, v1
	ds_read_b128 v[16:19], v75
	v_bitop3_b32 v0, v66, v0, 2 bitop3:0x36
	v_lshlrev_b32_e32 v1, 6, v67
	v_or_b32_e32 v79, v1, v2
	v_lshlrev_b32_e32 v25, 4, v0
	ds_read_b128 v[82:85], v79
	v_or_b32_e32 v80, v1, v25
	ds_read_b128 v[20:23], v80
	ds_read_b128 v[86:89], v75 offset:2048
	v_or_b32_e32 v24, v24, v25
	v_add_u32_e32 v77, 0x13700, v24
	ds_read_b128 v[90:93], v77
	ds_read_b128 v[98:101], v75 offset:16384
	s_waitcnt lgkmcnt(4)
	v_mfma_f32_32x32x16_f16 v[0:15], v[16:19], v[82:85], 0
	v_add_u32_e32 v52, 1, v67
	v_lshrrev_b32_e32 v94, 2, v52
	v_or_b32_e32 v96, 2, v66
	v_bitop3_b32 v81, v94, v66, 3 bitop3:0x6c
	v_lshlrev_b32_e32 v52, 6, v52
	v_lshl_or_b32 v81, v81, 4, v52
	s_waitcnt lgkmcnt(3)
	v_mfma_f32_32x32x16_f16 v[16:31], v[16:19], v[20:23], 0
	s_waitcnt lgkmcnt(1)
	v_mfma_f32_32x32x16_f16 v[16:31], v[90:93], v[82:85], v[16:31]
	v_bitop3_b32 v82, v94, v96, 3 bitop3:0x6c
	v_lshl_or_b32 v82, v82, 4, v52
	ds_read_b128 v[90:93], v81
	ds_read_b128 v[102:105], v82
	v_add_u32_e32 v52, 2, v67
	v_lshrrev_b32_e32 v94, 2, v52
	v_bitop3_b32 v83, v94, v66, 3 bitop3:0x6c
	s_waitcnt lgkmcnt(1)
	v_mfma_f32_32x32x16_f16 v[0:15], v[86:89], v[90:93], v[0:15]
	v_lshlrev_b32_e32 v52, 6, v52
	v_lshl_or_b32 v83, v83, 4, v52
	s_waitcnt lgkmcnt(0)
	v_mfma_f32_32x32x16_f16 v[16:31], v[86:89], v[102:105], v[16:31]
	ds_read_b128 v[84:87], v77 offset:2048
	ds_read_b128 v[102:105], v75 offset:4096
	ds_read_b128 v[106:109], v77 offset:4096
	s_waitcnt lgkmcnt(2)
	v_mfma_f32_32x32x16_f16 v[16:31], v[84:87], v[90:93], v[16:31]
	v_bitop3_b32 v84, v94, v96, 3 bitop3:0x6c
	v_lshl_or_b32 v84, v84, 4, v52
	ds_read_b128 v[86:89], v83
	ds_read_b128 v[90:93], v84
	ds_read_b128 v[110:113], v75 offset:6144
	v_add_u32_e32 v52, 0xb6, v67
	s_waitcnt lgkmcnt(1)
	v_mfma_f32_32x32x16_f16 v[16:31], v[102:105], v[90:93], v[16:31]
	v_lshrrev_b32_e32 v92, 2, v52
	v_lshlrev_b32_e32 v52, 6, v52
	v_bitop3_b32 v85, v92, v66, 3 bitop3:0x6c
	v_lshl_or_b32 v85, v85, 4, v52
	v_mfma_f32_32x32x16_f16 v[16:31], v[106:109], v[86:89], v[16:31]
	v_mfma_f32_32x32x16_f16 v[0:15], v[102:105], v[86:89], v[0:15]
	v_bitop3_b32 v86, v92, v96, 3 bitop3:0x6c
	v_lshl_or_b32 v86, v86, 4, v52
	ds_read_b128 v[92:95], v86
	ds_read_b128 v[88:91], v85
	v_add_u32_e32 v52, 0xb7, v67
	s_waitcnt lgkmcnt(1)
	v_mfma_f32_32x32x16_f16 v[16:31], v[110:113], v[92:95], v[16:31]
	ds_read_b128 v[92:95], v77 offset:6144
	ds_read_b128 v[102:105], v75 offset:8192
	ds_read_b128 v[106:109], v77 offset:8192
	s_waitcnt lgkmcnt(2)
	v_mfma_f32_32x32x16_f16 v[16:31], v[92:95], v[88:91], v[16:31]
	v_mfma_f32_32x32x16_f16 v[0:15], v[110:113], v[88:91], v[0:15]
	v_lshrrev_b32_e32 v110, 2, v52
	v_bitop3_b32 v87, v110, v66, 3 bitop3:0x6c
	v_lshlrev_b32_e32 v52, 6, v52
	v_bitop3_b32 v88, v110, v96, 3 bitop3:0x6c
	v_lshl_or_b32 v87, v87, 4, v52
	v_lshl_or_b32 v88, v88, 4, v52
	ds_read_b128 v[90:93], v87
	ds_read_b128 v[110:113], v88
	ds_read_b128 v[114:117], v75 offset:10240
	s_waitcnt lgkmcnt(1)
	v_mfma_f32_32x32x16_f16 v[16:31], v[102:105], v[110:113], v[16:31]
	v_add_u32_e32 v52, 0xb8, v67
	v_mfma_f32_32x32x16_f16 v[0:15], v[102:105], v[90:93], v[0:15]
	v_lshrrev_b32_e32 v102, 2, v52
	v_lshlrev_b32_e32 v52, 6, v52
	v_bitop3_b32 v89, v102, v66, 3 bitop3:0x6c
	v_lshl_or_b32 v89, v89, 4, v52
	v_mfma_f32_32x32x16_f16 v[16:31], v[106:109], v[90:93], v[16:31]
	v_bitop3_b32 v90, v102, v96, 3 bitop3:0x6c
	v_lshl_or_b32 v90, v90, 4, v52
	ds_read_b128 v[102:105], v90
	ds_read_b128 v[92:95], v89
	v_add_u32_e32 v52, 0x16c, v67
	s_waitcnt lgkmcnt(1)
	v_mfma_f32_32x32x16_f16 v[16:31], v[114:117], v[102:105], v[16:31]
	ds_read_b128 v[102:105], v77 offset:10240
	ds_read_b128 v[106:109], v75 offset:12288
	ds_read_b128 v[110:113], v77 offset:12288
	s_waitcnt lgkmcnt(2)
	v_mfma_f32_32x32x16_f16 v[16:31], v[102:105], v[92:95], v[16:31]
	v_mfma_f32_32x32x16_f16 v[0:15], v[114:117], v[92:95], v[0:15]
	v_lshrrev_b32_e32 v114, 2, v52
	v_bitop3_b32 v91, v114, v66, 3 bitop3:0x6c
	v_lshlrev_b32_e32 v52, 6, v52
	v_bitop3_b32 v92, v114, v96, 3 bitop3:0x6c
	v_lshl_or_b32 v91, v91, 4, v52
	v_lshl_or_b32 v92, v92, 4, v52
	ds_read_b128 v[102:105], v91
	ds_read_b128 v[114:117], v92
	ds_read_b128 v[118:121], v75 offset:14336
	s_waitcnt lgkmcnt(1)
	v_mfma_f32_32x32x16_f16 v[16:31], v[106:109], v[114:117], v[16:31]
	v_add_u32_e32 v52, 0x16d, v67
	v_lshrrev_b32_e32 v94, 2, v52
	v_bitop3_b32 v93, v94, v66, 3 bitop3:0x6c
	v_lshlrev_b32_e32 v52, 6, v52
	v_bitop3_b32 v94, v94, v96, 3 bitop3:0x6c
	v_lshl_or_b32 v93, v93, 4, v52
	v_lshl_or_b32 v94, v94, 4, v52
	v_mfma_f32_32x32x16_f16 v[16:31], v[110:113], v[102:105], v[16:31]
	v_add_u32_e32 v52, 0x16e, v67
	v_lshrrev_b32_e32 v114, 2, v52
	ds_read_b128 v[110:113], v77 offset:16384
	v_bitop3_b32 v95, v114, v66, 3 bitop3:0x6c
	v_lshlrev_b32_e32 v52, 6, v52
	v_bitop3_b32 v96, v114, v96, 3 bitop3:0x6c
	v_lshl_or_b32 v95, v95, 4, v52
	v_mfma_f32_32x32x16_f16 v[0:15], v[106:109], v[102:105], v[0:15]
	ds_read_b128 v[102:105], v93
	ds_read_b128 v[106:109], v94
	v_lshl_or_b32 v96, v96, 4, v52
	s_waitcnt lgkmcnt(0)
	v_mfma_f32_32x32x16_f16 v[16:31], v[118:121], v[106:109], v[16:31]
	ds_read_b128 v[106:109], v77 offset:14336
	s_waitcnt lgkmcnt(0)
	v_mfma_f32_32x32x16_f16 v[16:31], v[106:109], v[102:105], v[16:31]
	ds_read_b128 v[106:109], v96
	v_mfma_f32_32x32x16_f16 v[0:15], v[118:121], v[102:105], v[0:15]
	ds_read_b128 v[102:105], v95
	s_waitcnt vmcnt(4)
	ds_write_b128 v70, v[44:47] offset:39808
	ds_write_b128 v71, v[36:39] offset:39808
	ds_write_b128 v72, v[40:43] offset:39808
	s_waitcnt vmcnt(3)
	ds_write_b128 v73, v[48:51] offset:39808
	s_waitcnt lgkmcnt(5)
	v_mfma_f32_32x32x16_f16 v[16:31], v[98:101], v[106:109], v[16:31]
	s_waitcnt lgkmcnt(4)
	v_mfma_f32_32x32x16_f16 v[0:15], v[98:101], v[102:105], v[0:15]
	v_mfma_f32_32x32x16_f16 v[16:31], v[110:113], v[102:105], v[16:31]
	s_and_saveexec_b64 s[6:7], s[2:3]
	ds_write_b128 v69, v[32:35] offset:39808
	s_or_b64 exec, exec, s[6:7]
	v_mov_b32_e32 v32, 0x13700
	v_lshl_add_u32 v97, v97, 4, v32
	s_waitcnt vmcnt(2)
	ds_write_b128 v74, v[56:59] offset:18432
	s_waitcnt vmcnt(1)
	ds_write_b128 v97, v[60:63] offset:18432
	s_and_saveexec_b64 s[6:7], s[4:5]
	v_mov_b32_e32 v32, 0x17f00
	v_mov_b32_e32 v52, v65
	v_lshl_add_u32 v32, v68, 4, v32
	ds_write_b128 v32, v[52:55]
	s_or_b64 exec, exec, s[6:7]
	s_add_u32 s6, s8, 0x40c000
	s_addc_u32 s7, s9, 0
	v_mov_b32_e32 v65, 0
	v_lshl_add_u64 v[32:33], s[6:7], 0, v[64:65]
	v_add_co_u32_e32 v34, vcc, 0x2000, v32
	s_waitcnt lgkmcnt(0)
	s_nop 0
	v_addc_co_u32_e32 v35, vcc, 0, v33, vcc
	v_add_co_u32_e32 v32, vcc, 0x6000, v32
	s_barrier
	global_load_dwordx4 v[36:39], v[34:35], off
	global_load_dwordx4 v[40:43], v76, s[6:7]
	v_addc_co_u32_e32 v33, vcc, 0, v33, vcc
	global_load_dwordx4 v[44:47], v64, s[6:7]
	global_load_dwordx4 v[48:51], v[32:33], off
	v_mov_b32_e32 v32, v65
	v_mov_b32_e32 v33, v65
	v_mov_b32_e32 v34, v65
	v_mov_b32_e32 v35, v65
	s_and_saveexec_b64 s[12:13], s[2:3]
	s_cbranch_execz .LBB4_22
	global_load_dwordx4 v[32:35], v78, s[6:7]

.LBB4_24:
	s_or_b64 exec, exec, s[12:13]
	s_add_u32 s16, s8, 0x612000
	s_addc_u32 s17, s9, 0
	global_load_dword v124, v125, s[16:17]
	ds_read_b128 v[98:101], v75 offset:18432
	ds_read_b128 v[102:105], v79 offset:39808
	ds_read_b128 v[106:109], v80 offset:39808
	ds_read_b128 v[110:113], v75 offset:20480
	s_waitcnt lgkmcnt(2)
	v_mfma_f32_32x32x16_f16 v[0:15], v[98:101], v[102:105], v[0:15]
	s_waitcnt lgkmcnt(1)
	v_mfma_f32_32x32x16_f16 v[16:31], v[98:101], v[106:109], v[16:31]
	ds_read_b128 v[98:101], v77 offset:18432
	ds_read_b128 v[106:109], v77 offset:34816
	s_waitcnt lgkmcnt(1)
	v_mfma_f32_32x32x16_f16 v[16:31], v[98:101], v[102:105], v[16:31]
	ds_read_b128 v[98:101], v81 offset:39808
	ds_read_b128 v[102:105], v82 offset:39808
	s_waitcnt lgkmcnt(0)
	v_mfma_f32_32x32x16_f16 v[16:31], v[110:113], v[102:105], v[16:31]
	v_mfma_f32_32x32x16_f16 v[0:15], v[110:113], v[98:101], v[0:15]
	ds_read_b128 v[102:105], v77 offset:20480
	ds_read_b128 v[110:113], v77 offset:22528
	s_waitcnt lgkmcnt(1)
	v_mfma_f32_32x32x16_f16 v[16:31], v[102:105], v[98:101], v[16:31]
	ds_read_b128 v[98:101], v75 offset:22528
	ds_read_b128 v[102:105], v83 offset:39808
	ds_read_b128 v[114:117], v84 offset:39808
	ds_read_b128 v[118:121], v75 offset:24576
	s_waitcnt lgkmcnt(1)
	v_mfma_f32_32x32x16_f16 v[16:31], v[98:101], v[114:117], v[16:31]
	v_mfma_f32_32x32x16_f16 v[16:31], v[110:113], v[102:105], v[16:31]
	v_mfma_f32_32x32x16_f16 v[0:15], v[98:101], v[102:105], v[0:15]
	ds_read_b128 v[98:101], v85 offset:39808
	ds_read_b128 v[102:105], v86 offset:39808
	s_waitcnt lgkmcnt(0)
	v_mfma_f32_32x32x16_f16 v[16:31], v[118:121], v[102:105], v[16:31]
	ds_read_b128 v[102:105], v77 offset:24576
	ds_read_b128 v[110:113], v77 offset:26624
	s_waitcnt lgkmcnt(1)
	v_mfma_f32_32x32x16_f16 v[16:31], v[102:105], v[98:101], v[16:31]
	v_mfma_f32_32x32x16_f16 v[0:15], v[118:121], v[98:101], v[0:15]
	ds_read_b128 v[98:101], v75 offset:26624
	ds_read_b128 v[102:105], v87 offset:39808
	ds_read_b128 v[114:117], v88 offset:39808
	ds_read_b128 v[118:121], v75 offset:28672
	s_waitcnt lgkmcnt(1)
	v_mfma_f32_32x32x16_f16 v[16:31], v[98:101], v[114:117], v[16:31]
	v_mfma_f32_32x32x16_f16 v[16:31], v[110:113], v[102:105], v[16:31]
	v_mfma_f32_32x32x16_f16 v[0:15], v[98:101], v[102:105], v[0:15]
	ds_read_b128 v[98:101], v89 offset:39808
	ds_read_b128 v[102:105], v90 offset:39808
	s_waitcnt lgkmcnt(0)
	v_mfma_f32_32x32x16_f16 v[16:31], v[118:121], v[102:105], v[16:31]
	ds_read_b128 v[102:105], v77 offset:28672
	ds_read_b128 v[110:113], v77 offset:30720
	s_waitcnt lgkmcnt(1)
	v_mfma_f32_32x32x16_f16 v[16:31], v[102:105], v[98:101], v[16:31]
	v_mfma_f32_32x32x16_f16 v[0:15], v[118:121], v[98:101], v[0:15]
	ds_read_b128 v[98:101], v75 offset:30720
	ds_read_b128 v[102:105], v91 offset:39808
	ds_read_b128 v[114:117], v92 offset:39808
	ds_read_b128 v[118:121], v77 offset:32768
	s_waitcnt lgkmcnt(1)
	v_mfma_f32_32x32x16_f16 v[16:31], v[98:101], v[114:117], v[16:31]
	v_mfma_f32_32x32x16_f16 v[16:31], v[110:113], v[102:105], v[16:31]
	v_mfma_f32_32x32x16_f16 v[0:15], v[98:101], v[102:105], v[0:15]
	ds_read_b128 v[98:101], v75 offset:32768
	ds_read_b128 v[102:105], v93 offset:39808
	ds_read_b128 v[110:113], v94 offset:39808
	ds_read_b128 v[114:117], v75 offset:34816
	s_waitcnt lgkmcnt(1)
	v_mfma_f32_32x32x16_f16 v[16:31], v[98:101], v[110:113], v[16:31]
	v_mfma_f32_32x32x16_f16 v[16:31], v[118:121], v[102:105], v[16:31]
	v_mfma_f32_32x32x16_f16 v[0:15], v[98:101], v[102:105], v[0:15]
	ds_read_b128 v[98:101], v95 offset:39808
	ds_read_b128 v[102:105], v96 offset:39808
	s_waitcnt vmcnt(4)
	ds_write_b128 v70, v[44:47]
	ds_write_b128 v71, v[36:39]
	ds_write_b128 v72, v[40:43]
	s_waitcnt vmcnt(3)
	ds_write_b128 v73, v[48:51]
	s_waitcnt lgkmcnt(4)
	v_mfma_f32_32x32x16_f16 v[16:31], v[114:117], v[102:105], v[16:31]
	v_mfma_f32_32x32x16_f16 v[0:15], v[114:117], v[98:101], v[0:15]
	v_mfma_f32_32x32x16_f16 v[16:31], v[106:109], v[98:101], v[16:31]
	s_and_saveexec_b64 s[6:7], s[2:3]
	ds_write_b128 v69, v[32:35]
	s_or_b64 exec, exec, s[6:7]
	s_waitcnt vmcnt(2)
	ds_write_b128 v74, v[56:59]
	s_waitcnt vmcnt(1)
	ds_write_b128 v97, v[60:63]
	s_and_saveexec_b64 s[6:7], s[4:5]
	v_mov_b32_e32 v32, 0x13700
	v_mov_b32_e32 v52, v65
	v_lshl_add_u32 v32, v68, 4, v32
	ds_write_b128 v32, v[52:55]
	s_or_b64 exec, exec, s[6:7]
	s_add_u32 s6, s8, 0x612000
	s_addc_u32 s7, s9, 0
	v_mov_b32_e32 v65, 0
	v_lshl_add_u64 v[32:33], s[6:7], 0, v[64:65]
	v_add_co_u32_e32 v34, vcc, 0x2000, v32
	s_waitcnt lgkmcnt(0)
	s_nop 0
	v_addc_co_u32_e32 v35, vcc, 0, v33, vcc
	v_add_co_u32_e32 v32, vcc, 0x6000, v32
	s_barrier
	global_load_dwordx4 v[36:39], v[34:35], off
	global_load_dwordx4 v[40:43], v76, s[6:7]
	v_addc_co_u32_e32 v33, vcc, 0, v33, vcc
	global_load_dwordx4 v[44:47], v64, s[6:7]
	global_load_dwordx4 v[48:51], v[32:33], off
	v_mov_b32_e32 v32, v65
	v_mov_b32_e32 v33, v65
	v_mov_b32_e32 v34, v65
	v_mov_b32_e32 v35, v65
	s_and_saveexec_b64 s[12:13], s[2:3]
	s_cbranch_execz .LBB4_30
	global_load_dwordx4 v[32:35], v78, s[6:7]

.LBB4_32:
	s_or_b64 exec, exec, s[12:13]
	s_add_u32 s16, s8, 0x818000
	s_addc_u32 s17, s9, 0
	global_load_dword v124, v125, s[16:17]
	ds_read_b128 v[98:101], v75
	ds_read_b128 v[102:105], v79
	ds_read_b128 v[106:109], v80
	ds_read_b128 v[110:113], v75 offset:2048
	s_waitcnt lgkmcnt(2)
	v_mfma_f32_32x32x16_f16 v[0:15], v[98:101], v[102:105], v[0:15]
	s_waitcnt lgkmcnt(1)
	v_mfma_f32_32x32x16_f16 v[16:31], v[98:101], v[106:109], v[16:31]
	ds_read_b128 v[98:101], v77
	ds_read_b128 v[106:109], v75 offset:16384
	s_waitcnt lgkmcnt(1)
	v_mfma_f32_32x32x16_f16 v[16:31], v[98:101], v[102:105], v[16:31]
	ds_read_b128 v[98:101], v81
	ds_read_b128 v[102:105], v82
	s_waitcnt lgkmcnt(0)
	v_mfma_f32_32x32x16_f16 v[16:31], v[110:113], v[102:105], v[16:31]
	v_mfma_f32_32x32x16_f16 v[0:15], v[110:113], v[98:101], v[0:15]
	ds_read_b128 v[102:105], v77 offset:2048
	ds_read_b128 v[110:113], v77 offset:4096
	s_waitcnt lgkmcnt(1)
	v_mfma_f32_32x32x16_f16 v[16:31], v[102:105], v[98:101], v[16:31]
	ds_read_b128 v[98:101], v75 offset:4096
	ds_read_b128 v[102:105], v83
	ds_read_b128 v[114:117], v84
	ds_read_b128 v[118:121], v75 offset:6144
	s_waitcnt lgkmcnt(1)
	v_mfma_f32_32x32x16_f16 v[16:31], v[98:101], v[114:117], v[16:31]
	v_mfma_f32_32x32x16_f16 v[16:31], v[110:113], v[102:105], v[16:31]
	v_mfma_f32_32x32x16_f16 v[0:15], v[98:101], v[102:105], v[0:15]
	ds_read_b128 v[98:101], v85
	ds_read_b128 v[102:105], v86
	s_waitcnt lgkmcnt(0)
	v_mfma_f32_32x32x16_f16 v[16:31], v[118:121], v[102:105], v[16:31]
	ds_read_b128 v[102:105], v77 offset:6144
	ds_read_b128 v[110:113], v77 offset:8192
	s_waitcnt lgkmcnt(1)
	v_mfma_f32_32x32x16_f16 v[16:31], v[102:105], v[98:101], v[16:31]
	v_mfma_f32_32x32x16_f16 v[0:15], v[118:121], v[98:101], v[0:15]
	ds_read_b128 v[98:101], v75 offset:8192
	ds_read_b128 v[102:105], v87
	ds_read_b128 v[114:117], v88
	ds_read_b128 v[118:121], v75 offset:10240
	s_waitcnt lgkmcnt(1)
	v_mfma_f32_32x32x16_f16 v[16:31], v[98:101], v[114:117], v[16:31]
	v_mfma_f32_32x32x16_f16 v[16:31], v[110:113], v[102:105], v[16:31]
	v_mfma_f32_32x32x16_f16 v[0:15], v[98:101], v[102:105], v[0:15]
	ds_read_b128 v[98:101], v89
	ds_read_b128 v[102:105], v90
	s_waitcnt lgkmcnt(0)
	v_mfma_f32_32x32x16_f16 v[16:31], v[118:121], v[102:105], v[16:31]
	ds_read_b128 v[102:105], v77 offset:10240
	ds_read_b128 v[110:113], v77 offset:12288
	s_waitcnt lgkmcnt(1)
	v_mfma_f32_32x32x16_f16 v[16:31], v[102:105], v[98:101], v[16:31]
	v_mfma_f32_32x32x16_f16 v[0:15], v[118:121], v[98:101], v[0:15]
	ds_read_b128 v[98:101], v75 offset:12288
	ds_read_b128 v[102:105], v91
	ds_read_b128 v[114:117], v92
	ds_read_b128 v[118:121], v75 offset:14336
	s_waitcnt lgkmcnt(1)
	v_mfma_f32_32x32x16_f16 v[16:31], v[98:101], v[114:117], v[16:31]
	v_mfma_f32_32x32x16_f16 v[16:31], v[110:113], v[102:105], v[16:31]
	v_mfma_f32_32x32x16_f16 v[0:15], v[98:101], v[102:105], v[0:15]
	ds_read_b128 v[98:101], v93
	ds_read_b128 v[102:105], v94
	s_waitcnt lgkmcnt(0)
	v_mfma_f32_32x32x16_f16 v[16:31], v[118:121], v[102:105], v[16:31]
	ds_read_b128 v[102:105], v77 offset:14336
	ds_read_b128 v[110:113], v77 offset:16384
	s_waitcnt lgkmcnt(1)
	v_mfma_f32_32x32x16_f16 v[16:31], v[102:105], v[98:101], v[16:31]
	v_mfma_f32_32x32x16_f16 v[0:15], v[118:121], v[98:101], v[0:15]
	ds_read_b128 v[98:101], v95
	ds_read_b128 v[102:105], v96
	s_waitcnt vmcnt(4)
	ds_write_b128 v70, v[44:47] offset:39808
	ds_write_b128 v71, v[36:39] offset:39808
	ds_write_b128 v72, v[40:43] offset:39808
	s_waitcnt vmcnt(3)
	ds_write_b128 v73, v[48:51] offset:39808
	s_waitcnt lgkmcnt(4)
	v_mfma_f32_32x32x16_f16 v[16:31], v[106:109], v[102:105], v[16:31]
	v_mfma_f32_32x32x16_f16 v[0:15], v[106:109], v[98:101], v[0:15]
	v_mfma_f32_32x32x16_f16 v[16:31], v[110:113], v[98:101], v[16:31]
	s_and_saveexec_b64 s[6:7], s[2:3]
	ds_write_b128 v69, v[32:35] offset:39808
	s_or_b64 exec, exec, s[6:7]
	s_waitcnt vmcnt(2)
	ds_write_b128 v74, v[56:59] offset:18432
	s_waitcnt vmcnt(1)
	ds_write_b128 v97, v[60:63] offset:18432
	s_and_saveexec_b64 s[6:7], s[4:5]
	v_mov_b32_e32 v32, 0x17f00
	v_mov_b32_e32 v52, v65
	v_lshl_add_u32 v32, v68, 4, v32
	ds_write_b128 v32, v[52:55]
	s_or_b64 exec, exec, s[6:7]
	s_add_u32 s6, s8, 0x818000
	s_addc_u32 s7, s9, 0
	v_mov_b32_e32 v65, 0
	v_lshl_add_u64 v[32:33], s[6:7], 0, v[64:65]
	v_add_co_u32_e32 v34, vcc, 0x2000, v32
	s_waitcnt lgkmcnt(0)
	s_nop 0
	v_addc_co_u32_e32 v35, vcc, 0, v33, vcc
	v_add_co_u32_e32 v32, vcc, 0x6000, v32
	s_barrier
	global_load_dwordx4 v[36:39], v[34:35], off
	global_load_dwordx4 v[40:43], v76, s[6:7]
	v_addc_co_u32_e32 v33, vcc, 0, v33, vcc
	global_load_dwordx4 v[44:47], v64, s[6:7]
	global_load_dwordx4 v[48:51], v[32:33], off
	v_mov_b32_e32 v32, v65
	v_mov_b32_e32 v33, v65
	v_mov_b32_e32 v34, v65
	v_mov_b32_e32 v35, v65
	s_and_saveexec_b64 s[12:13], s[2:3]
	s_cbranch_execz .LBB4_38
	global_load_dwordx4 v[32:35], v78, s[6:7]

.LBB4_40:
	s_or_b64 exec, exec, s[12:13]
	s_add_u32 s16, s8, 0xa1e000
	s_addc_u32 s17, s9, 0
	global_load_dword v124, v125, s[16:17]
	ds_read_b128 v[98:101], v75 offset:18432
	ds_read_b128 v[102:105], v79 offset:39808
	ds_read_b128 v[106:109], v80 offset:39808
	ds_read_b128 v[110:113], v75 offset:20480
	s_waitcnt lgkmcnt(2)
	v_mfma_f32_32x32x16_f16 v[0:15], v[98:101], v[102:105], v[0:15]
	s_waitcnt lgkmcnt(1)
	v_mfma_f32_32x32x16_f16 v[16:31], v[98:101], v[106:109], v[16:31]
	ds_read_b128 v[98:101], v77 offset:18432
	ds_read_b128 v[106:109], v77 offset:34816
	s_waitcnt lgkmcnt(1)
	v_mfma_f32_32x32x16_f16 v[16:31], v[98:101], v[102:105], v[16:31]
	ds_read_b128 v[98:101], v81 offset:39808
	ds_read_b128 v[102:105], v82 offset:39808
	s_waitcnt lgkmcnt(0)
	v_mfma_f32_32x32x16_f16 v[16:31], v[110:113], v[102:105], v[16:31]
	v_mfma_f32_32x32x16_f16 v[0:15], v[110:113], v[98:101], v[0:15]
	ds_read_b128 v[102:105], v77 offset:20480
	ds_read_b128 v[110:113], v77 offset:22528
	s_waitcnt lgkmcnt(1)
	v_mfma_f32_32x32x16_f16 v[16:31], v[102:105], v[98:101], v[16:31]
	ds_read_b128 v[98:101], v75 offset:22528
	ds_read_b128 v[102:105], v83 offset:39808
	ds_read_b128 v[114:117], v84 offset:39808
	ds_read_b128 v[118:121], v75 offset:24576
	s_waitcnt lgkmcnt(1)
	v_mfma_f32_32x32x16_f16 v[16:31], v[98:101], v[114:117], v[16:31]
	v_mfma_f32_32x32x16_f16 v[16:31], v[110:113], v[102:105], v[16:31]
	v_mfma_f32_32x32x16_f16 v[0:15], v[98:101], v[102:105], v[0:15]
	ds_read_b128 v[98:101], v85 offset:39808
	ds_read_b128 v[102:105], v86 offset:39808
	s_waitcnt lgkmcnt(0)
	v_mfma_f32_32x32x16_f16 v[16:31], v[118:121], v[102:105], v[16:31]
	ds_read_b128 v[102:105], v77 offset:24576
	ds_read_b128 v[110:113], v77 offset:26624
	s_waitcnt lgkmcnt(1)
	v_mfma_f32_32x32x16_f16 v[16:31], v[102:105], v[98:101], v[16:31]
	v_mfma_f32_32x32x16_f16 v[0:15], v[118:121], v[98:101], v[0:15]
	ds_read_b128 v[98:101], v75 offset:26624
	ds_read_b128 v[102:105], v87 offset:39808
	ds_read_b128 v[114:117], v88 offset:39808
	ds_read_b128 v[118:121], v75 offset:28672
	s_waitcnt lgkmcnt(1)
	v_mfma_f32_32x32x16_f16 v[16:31], v[98:101], v[114:117], v[16:31]
	v_mfma_f32_32x32x16_f16 v[16:31], v[110:113], v[102:105], v[16:31]
	v_mfma_f32_32x32x16_f16 v[0:15], v[98:101], v[102:105], v[0:15]
	ds_read_b128 v[98:101], v89 offset:39808
	ds_read_b128 v[102:105], v90 offset:39808
	s_waitcnt lgkmcnt(0)
	v_mfma_f32_32x32x16_f16 v[16:31], v[118:121], v[102:105], v[16:31]
	ds_read_b128 v[102:105], v77 offset:28672
	ds_read_b128 v[110:113], v77 offset:30720
	s_waitcnt lgkmcnt(1)
	v_mfma_f32_32x32x16_f16 v[16:31], v[102:105], v[98:101], v[16:31]
	v_mfma_f32_32x32x16_f16 v[0:15], v[118:121], v[98:101], v[0:15]
	ds_read_b128 v[98:101], v75 offset:30720
	ds_read_b128 v[102:105], v91 offset:39808
	ds_read_b128 v[114:117], v92 offset:39808
	ds_read_b128 v[118:121], v77 offset:32768
	s_waitcnt lgkmcnt(1)
	v_mfma_f32_32x32x16_f16 v[16:31], v[98:101], v[114:117], v[16:31]
	v_mfma_f32_32x32x16_f16 v[16:31], v[110:113], v[102:105], v[16:31]
	v_mfma_f32_32x32x16_f16 v[0:15], v[98:101], v[102:105], v[0:15]
	ds_read_b128 v[98:101], v75 offset:32768
	ds_read_b128 v[102:105], v93 offset:39808
	ds_read_b128 v[110:113], v94 offset:39808
	ds_read_b128 v[114:117], v75 offset:34816
	s_waitcnt lgkmcnt(1)
	v_mfma_f32_32x32x16_f16 v[16:31], v[98:101], v[110:113], v[16:31]
	v_mfma_f32_32x32x16_f16 v[16:31], v[118:121], v[102:105], v[16:31]
	v_mfma_f32_32x32x16_f16 v[0:15], v[98:101], v[102:105], v[0:15]
	ds_read_b128 v[98:101], v95 offset:39808
	ds_read_b128 v[102:105], v96 offset:39808
	s_waitcnt vmcnt(4)
	ds_write_b128 v70, v[44:47]
	ds_write_b128 v71, v[36:39]
	ds_write_b128 v72, v[40:43]
	s_waitcnt vmcnt(3)
	ds_write_b128 v73, v[48:51]
	s_waitcnt lgkmcnt(4)
	v_mfma_f32_32x32x16_f16 v[16:31], v[114:117], v[102:105], v[16:31]
	v_mfma_f32_32x32x16_f16 v[0:15], v[114:117], v[98:101], v[0:15]
	v_mfma_f32_32x32x16_f16 v[16:31], v[106:109], v[98:101], v[16:31]
	s_and_saveexec_b64 s[6:7], s[2:3]
	ds_write_b128 v69, v[32:35]
	s_or_b64 exec, exec, s[6:7]
	s_waitcnt vmcnt(2)
	ds_write_b128 v74, v[56:59]
	s_waitcnt vmcnt(1)
	ds_write_b128 v97, v[60:63]
	s_and_saveexec_b64 s[6:7], s[4:5]
	v_mov_b32_e32 v32, 0x13700
	v_mov_b32_e32 v52, v65
	v_lshl_add_u32 v32, v68, 4, v32
	ds_write_b128 v32, v[52:55]
	s_or_b64 exec, exec, s[6:7]
	s_add_u32 s6, s8, 0xa1e000
	s_addc_u32 s7, s9, 0
	v_mov_b32_e32 v65, 0
	v_lshl_add_u64 v[32:33], s[6:7], 0, v[64:65]
	v_add_co_u32_e32 v34, vcc, 0x2000, v32
	s_waitcnt lgkmcnt(0)
	s_nop 0
	v_addc_co_u32_e32 v35, vcc, 0, v33, vcc
	v_add_co_u32_e32 v32, vcc, 0x6000, v32
	s_barrier
	global_load_dwordx4 v[36:39], v[34:35], off
	global_load_dwordx4 v[40:43], v76, s[6:7]
	v_addc_co_u32_e32 v33, vcc, 0, v33, vcc
	global_load_dwordx4 v[44:47], v64, s[6:7]
	global_load_dwordx4 v[48:51], v[32:33], off
	v_mov_b32_e32 v32, v65
	v_mov_b32_e32 v33, v65
	v_mov_b32_e32 v34, v65
	v_mov_b32_e32 v35, v65
	s_and_saveexec_b64 s[12:13], s[2:3]
	s_cbranch_execz .LBB4_46
	global_load_dwordx4 v[32:35], v78, s[6:7]

.LBB4_48:
	s_or_b64 exec, exec, s[12:13]
	s_add_u32 s16, s8, 0xc24000
	s_addc_u32 s17, s9, 0
	global_load_dword v124, v125, s[16:17]
	ds_read_b128 v[98:101], v75
	ds_read_b128 v[102:105], v79
	ds_read_b128 v[106:109], v80
	ds_read_b128 v[110:113], v75 offset:2048
	s_waitcnt lgkmcnt(2)
	v_mfma_f32_32x32x16_f16 v[0:15], v[98:101], v[102:105], v[0:15]
	s_waitcnt lgkmcnt(1)
	v_mfma_f32_32x32x16_f16 v[16:31], v[98:101], v[106:109], v[16:31]
	ds_read_b128 v[98:101], v77
	ds_read_b128 v[106:109], v75 offset:16384
	s_waitcnt lgkmcnt(1)
	v_mfma_f32_32x32x16_f16 v[16:31], v[98:101], v[102:105], v[16:31]
	ds_read_b128 v[98:101], v81
	ds_read_b128 v[102:105], v82
	s_waitcnt lgkmcnt(0)
	v_mfma_f32_32x32x16_f16 v[16:31], v[110:113], v[102:105], v[16:31]
	v_mfma_f32_32x32x16_f16 v[0:15], v[110:113], v[98:101], v[0:15]
	ds_read_b128 v[102:105], v77 offset:2048
	ds_read_b128 v[110:113], v77 offset:4096
	s_waitcnt lgkmcnt(1)
	v_mfma_f32_32x32x16_f16 v[16:31], v[102:105], v[98:101], v[16:31]
	ds_read_b128 v[98:101], v75 offset:4096
	ds_read_b128 v[102:105], v83
	ds_read_b128 v[114:117], v84
	ds_read_b128 v[118:121], v75 offset:6144
	s_waitcnt lgkmcnt(1)
	v_mfma_f32_32x32x16_f16 v[16:31], v[98:101], v[114:117], v[16:31]
	v_mfma_f32_32x32x16_f16 v[16:31], v[110:113], v[102:105], v[16:31]
	v_mfma_f32_32x32x16_f16 v[0:15], v[98:101], v[102:105], v[0:15]
	ds_read_b128 v[98:101], v85
	ds_read_b128 v[102:105], v86
	s_waitcnt lgkmcnt(0)
	v_mfma_f32_32x32x16_f16 v[16:31], v[118:121], v[102:105], v[16:31]
	ds_read_b128 v[102:105], v77 offset:6144
	ds_read_b128 v[110:113], v77 offset:8192
	s_waitcnt lgkmcnt(1)
	v_mfma_f32_32x32x16_f16 v[16:31], v[102:105], v[98:101], v[16:31]
	v_mfma_f32_32x32x16_f16 v[0:15], v[118:121], v[98:101], v[0:15]
	ds_read_b128 v[98:101], v75 offset:8192
	ds_read_b128 v[102:105], v87
	ds_read_b128 v[114:117], v88
	ds_read_b128 v[118:121], v75 offset:10240
	s_waitcnt lgkmcnt(1)
	v_mfma_f32_32x32x16_f16 v[16:31], v[98:101], v[114:117], v[16:31]
	v_mfma_f32_32x32x16_f16 v[16:31], v[110:113], v[102:105], v[16:31]
	v_mfma_f32_32x32x16_f16 v[0:15], v[98:101], v[102:105], v[0:15]
	ds_read_b128 v[98:101], v89
	ds_read_b128 v[102:105], v90
	s_waitcnt lgkmcnt(0)
	v_mfma_f32_32x32x16_f16 v[16:31], v[118:121], v[102:105], v[16:31]
	ds_read_b128 v[102:105], v77 offset:10240
	ds_read_b128 v[110:113], v77 offset:12288
	s_waitcnt lgkmcnt(1)
	v_mfma_f32_32x32x16_f16 v[16:31], v[102:105], v[98:101], v[16:31]
	v_mfma_f32_32x32x16_f16 v[0:15], v[118:121], v[98:101], v[0:15]
	ds_read_b128 v[98:101], v75 offset:12288
	ds_read_b128 v[102:105], v91
	ds_read_b128 v[114:117], v92
	ds_read_b128 v[118:121], v75 offset:14336
	s_waitcnt lgkmcnt(1)
	v_mfma_f32_32x32x16_f16 v[16:31], v[98:101], v[114:117], v[16:31]
	v_mfma_f32_32x32x16_f16 v[16:31], v[110:113], v[102:105], v[16:31]
	v_mfma_f32_32x32x16_f16 v[0:15], v[98:101], v[102:105], v[0:15]
	ds_read_b128 v[98:101], v93
	ds_read_b128 v[102:105], v94
	s_waitcnt lgkmcnt(0)
	v_mfma_f32_32x32x16_f16 v[16:31], v[118:121], v[102:105], v[16:31]
	ds_read_b128 v[102:105], v77 offset:14336
	ds_read_b128 v[110:113], v77 offset:16384
	s_waitcnt lgkmcnt(1)
	v_mfma_f32_32x32x16_f16 v[16:31], v[102:105], v[98:101], v[16:31]
	v_mfma_f32_32x32x16_f16 v[0:15], v[118:121], v[98:101], v[0:15]
	ds_read_b128 v[98:101], v95
	ds_read_b128 v[102:105], v96
	s_waitcnt vmcnt(4)
	ds_write_b128 v70, v[44:47] offset:39808
	ds_write_b128 v71, v[36:39] offset:39808
	ds_write_b128 v72, v[40:43] offset:39808
	s_waitcnt vmcnt(3)
	ds_write_b128 v73, v[48:51] offset:39808
	s_waitcnt lgkmcnt(4)
	v_mfma_f32_32x32x16_f16 v[16:31], v[106:109], v[102:105], v[16:31]
	v_mfma_f32_32x32x16_f16 v[0:15], v[106:109], v[98:101], v[0:15]
	v_mfma_f32_32x32x16_f16 v[16:31], v[110:113], v[98:101], v[16:31]
	s_and_saveexec_b64 s[6:7], s[2:3]
	ds_write_b128 v69, v[32:35] offset:39808
	s_or_b64 exec, exec, s[6:7]
	s_waitcnt vmcnt(2)
	ds_write_b128 v74, v[56:59] offset:18432
	s_waitcnt vmcnt(1)
	ds_write_b128 v97, v[60:63] offset:18432
	s_and_saveexec_b64 s[6:7], s[4:5]
	v_mov_b32_e32 v32, 0x17f00
	v_mov_b32_e32 v52, v65
	v_lshl_add_u32 v32, v68, 4, v32
	ds_write_b128 v32, v[52:55]
	s_or_b64 exec, exec, s[6:7]
	s_add_u32 s6, s8, 0xc24000
	s_addc_u32 s7, s9, 0
	v_mov_b32_e32 v65, 0
	v_lshl_add_u64 v[32:33], s[6:7], 0, v[64:65]
	v_add_co_u32_e32 v34, vcc, 0x2000, v32
	s_waitcnt lgkmcnt(0)
	s_nop 0
	v_addc_co_u32_e32 v35, vcc, 0, v33, vcc
	v_add_co_u32_e32 v32, vcc, 0x6000, v32
	s_barrier
	global_load_dwordx4 v[36:39], v[34:35], off
	global_load_dwordx4 v[40:43], v76, s[6:7]
	v_addc_co_u32_e32 v33, vcc, 0, v33, vcc
	global_load_dwordx4 v[44:47], v64, s[6:7]
	global_load_dwordx4 v[48:51], v[32:33], off
	v_mov_b32_e32 v32, v65
	v_mov_b32_e32 v33, v65
	v_mov_b32_e32 v34, v65
	v_mov_b32_e32 v35, v65
	s_and_saveexec_b64 s[12:13], s[2:3]
	s_cbranch_execz .LBB4_54
	global_load_dwordx4 v[32:35], v78, s[6:7]

.LBB4_56:
	s_or_b64 exec, exec, s[12:13]
	s_add_u32 s16, s8, 0xe2a000
	s_addc_u32 s17, s9, 0
	global_load_dword v124, v125, s[16:17]
	ds_read_b128 v[98:101], v75 offset:18432
	ds_read_b128 v[102:105], v79 offset:39808
	ds_read_b128 v[106:109], v80 offset:39808
	ds_read_b128 v[110:113], v75 offset:20480
	s_waitcnt lgkmcnt(2)
	v_mfma_f32_32x32x16_f16 v[0:15], v[98:101], v[102:105], v[0:15]
	s_waitcnt lgkmcnt(1)
	v_mfma_f32_32x32x16_f16 v[16:31], v[98:101], v[106:109], v[16:31]
	ds_read_b128 v[98:101], v77 offset:18432
	ds_read_b128 v[106:109], v77 offset:34816
	s_waitcnt lgkmcnt(1)
	v_mfma_f32_32x32x16_f16 v[16:31], v[98:101], v[102:105], v[16:31]
	ds_read_b128 v[98:101], v81 offset:39808
	ds_read_b128 v[102:105], v82 offset:39808
	s_waitcnt lgkmcnt(0)
	v_mfma_f32_32x32x16_f16 v[16:31], v[110:113], v[102:105], v[16:31]
	v_mfma_f32_32x32x16_f16 v[0:15], v[110:113], v[98:101], v[0:15]
	ds_read_b128 v[102:105], v77 offset:20480
	ds_read_b128 v[110:113], v77 offset:22528
	s_waitcnt lgkmcnt(1)
	v_mfma_f32_32x32x16_f16 v[16:31], v[102:105], v[98:101], v[16:31]
	ds_read_b128 v[98:101], v75 offset:22528
	ds_read_b128 v[102:105], v83 offset:39808
	ds_read_b128 v[114:117], v84 offset:39808
	ds_read_b128 v[118:121], v75 offset:24576
	s_waitcnt lgkmcnt(1)
	v_mfma_f32_32x32x16_f16 v[16:31], v[98:101], v[114:117], v[16:31]
	v_mfma_f32_32x32x16_f16 v[16:31], v[110:113], v[102:105], v[16:31]
	v_mfma_f32_32x32x16_f16 v[0:15], v[98:101], v[102:105], v[0:15]
	ds_read_b128 v[98:101], v85 offset:39808
	ds_read_b128 v[102:105], v86 offset:39808
	s_waitcnt lgkmcnt(0)
	v_mfma_f32_32x32x16_f16 v[16:31], v[118:121], v[102:105], v[16:31]
	ds_read_b128 v[102:105], v77 offset:24576
	ds_read_b128 v[110:113], v77 offset:26624
	s_waitcnt lgkmcnt(1)
	v_mfma_f32_32x32x16_f16 v[16:31], v[102:105], v[98:101], v[16:31]
	v_mfma_f32_32x32x16_f16 v[0:15], v[118:121], v[98:101], v[0:15]
	ds_read_b128 v[98:101], v75 offset:26624
	ds_read_b128 v[102:105], v87 offset:39808
	ds_read_b128 v[114:117], v88 offset:39808
	ds_read_b128 v[118:121], v75 offset:28672
	s_waitcnt lgkmcnt(1)
	v_mfma_f32_32x32x16_f16 v[16:31], v[98:101], v[114:117], v[16:31]
	v_mfma_f32_32x32x16_f16 v[16:31], v[110:113], v[102:105], v[16:31]
	v_mfma_f32_32x32x16_f16 v[0:15], v[98:101], v[102:105], v[0:15]
	ds_read_b128 v[98:101], v89 offset:39808
	ds_read_b128 v[102:105], v90 offset:39808
	s_waitcnt lgkmcnt(0)
	v_mfma_f32_32x32x16_f16 v[16:31], v[118:121], v[102:105], v[16:31]
	ds_read_b128 v[102:105], v77 offset:28672
	ds_read_b128 v[110:113], v77 offset:30720
	s_waitcnt lgkmcnt(1)
	v_mfma_f32_32x32x16_f16 v[16:31], v[102:105], v[98:101], v[16:31]
	v_mfma_f32_32x32x16_f16 v[0:15], v[118:121], v[98:101], v[0:15]
	ds_read_b128 v[98:101], v75 offset:30720
	ds_read_b128 v[102:105], v91 offset:39808
	ds_read_b128 v[114:117], v92 offset:39808
	ds_read_b128 v[118:121], v77 offset:32768
	s_waitcnt lgkmcnt(1)
	v_mfma_f32_32x32x16_f16 v[16:31], v[98:101], v[114:117], v[16:31]
	v_mfma_f32_32x32x16_f16 v[16:31], v[110:113], v[102:105], v[16:31]
	v_mfma_f32_32x32x16_f16 v[0:15], v[98:101], v[102:105], v[0:15]
	ds_read_b128 v[98:101], v75 offset:32768
	ds_read_b128 v[102:105], v93 offset:39808
	ds_read_b128 v[110:113], v94 offset:39808
	ds_read_b128 v[114:117], v75 offset:34816
	s_waitcnt lgkmcnt(1)
	v_mfma_f32_32x32x16_f16 v[16:31], v[98:101], v[110:113], v[16:31]
	v_mfma_f32_32x32x16_f16 v[16:31], v[118:121], v[102:105], v[16:31]
	v_mfma_f32_32x32x16_f16 v[0:15], v[98:101], v[102:105], v[0:15]
	ds_read_b128 v[98:101], v95 offset:39808
	ds_read_b128 v[102:105], v96 offset:39808
	s_waitcnt vmcnt(4)
	ds_write_b128 v70, v[44:47]
	ds_write_b128 v71, v[36:39]
	ds_write_b128 v72, v[40:43]
	s_waitcnt vmcnt(3)
	ds_write_b128 v73, v[48:51]
	s_waitcnt lgkmcnt(4)
	v_mfma_f32_32x32x16_f16 v[16:31], v[114:117], v[102:105], v[16:31]
	v_mfma_f32_32x32x16_f16 v[0:15], v[114:117], v[98:101], v[0:15]
	v_mfma_f32_32x32x16_f16 v[16:31], v[106:109], v[98:101], v[16:31]
	s_and_saveexec_b64 s[6:7], s[2:3]
	ds_write_b128 v69, v[32:35]
	s_or_b64 exec, exec, s[6:7]
	s_waitcnt vmcnt(2)
	ds_write_b128 v74, v[56:59]
	s_waitcnt vmcnt(1)
	ds_write_b128 v97, v[60:63]
	s_and_saveexec_b64 s[6:7], s[4:5]
	v_mov_b32_e32 v32, 0x13700
	v_mov_b32_e32 v52, v65
	v_lshl_add_u32 v32, v68, 4, v32
	ds_write_b128 v32, v[52:55]
	s_or_b64 exec, exec, s[6:7]
	s_add_u32 s6, s8, 0xe2a000
	s_addc_u32 s7, s9, 0
	v_mov_b32_e32 v65, 0
	v_lshl_add_u64 v[32:33], s[6:7], 0, v[64:65]
	v_add_co_u32_e32 v34, vcc, 0x2000, v32
	s_waitcnt lgkmcnt(0)
	s_nop 0
	v_addc_co_u32_e32 v35, vcc, 0, v33, vcc
	v_add_co_u32_e32 v32, vcc, 0x6000, v32
	s_barrier
	global_load_dwordx4 v[36:39], v[34:35], off
	global_load_dwordx4 v[40:43], v76, s[6:7]
	v_addc_co_u32_e32 v33, vcc, 0, v33, vcc
	global_load_dwordx4 v[44:47], v64, s[6:7]
	global_load_dwordx4 v[48:51], v[32:33], off
	v_mov_b32_e32 v32, v65
	v_mov_b32_e32 v33, v65
	v_mov_b32_e32 v34, v65
	v_mov_b32_e32 v35, v65
	s_and_saveexec_b64 s[8:9], s[2:3]
	s_cbranch_execz .LBB4_62
	global_load_dwordx4 v[32:35], v78, s[6:7]

	.amdhsa_kernel _Z12conv3_kernelPK15HIP_vector_typeIjLj4EES2_PKfPfS5_
		.amdhsa_group_segment_fixed_size 116480
		.amdhsa_private_segment_fixed_size 0
		.amdhsa_kernarg_size 40
		.amdhsa_user_sgpr_count 2
		.amdhsa_user_sgpr_dispatch_ptr 0
		.amdhsa_user_sgpr_queue_ptr 0
		.amdhsa_user_sgpr_kernarg_segment_ptr 1
		.amdhsa_user_sgpr_dispatch_id 0
		.amdhsa_user_sgpr_kernarg_preload_length 0
		.amdhsa_user_sgpr_kernarg_preload_offset 0
		.amdhsa_user_sgpr_private_segment_size 0
		.amdhsa_uses_dynamic_stack 0
		.amdhsa_enable_private_segment 0
		.amdhsa_system_sgpr_workgroup_id_x 1
		.amdhsa_system_sgpr_workgroup_id_y 1
		.amdhsa_system_sgpr_workgroup_id_z 0
		.amdhsa_system_sgpr_workgroup_info 0
		.amdhsa_system_vgpr_workitem_id 0
		.amdhsa_next_free_vgpr 169
		.amdhsa_next_free_sgpr 96
		.amdhsa_accum_offset 128
		.amdhsa_reserve_vcc 1
		.amdhsa_float_round_mode_32 0
		.amdhsa_float_round_mode_16_64 0
		.amdhsa_float_denorm_mode_32 3
		.amdhsa_float_denorm_mode_16_64 3
		.amdhsa_dx10_clamp 1
		.amdhsa_ieee_mode 1
		.amdhsa_fp16_overflow 0
		.amdhsa_tg_split 0
		.amdhsa_exception_fp_ieee_invalid_op 0
		.amdhsa_exception_fp_denorm_src 0
		.amdhsa_exception_fp_ieee_div_zero 0
		.amdhsa_exception_fp_ieee_overflow 0
		.amdhsa_exception_fp_ieee_underflow 0
		.amdhsa_exception_fp_ieee_inexact 0
		.amdhsa_exception_int_div_zero 0
	.end_amdhsa_kernel

amdhsa.kernels:
  - .agpr_count:     0
    .args:
      - .actual_access:  read_only
        .address_space:  global
        .offset:         0
        .size:           8
        .value_kind:     global_buffer
      - .actual_access:  write_only
        .address_space:  global
        .offset:         8
        .size:           8
        .value_kind:     global_buffer
    .group_segment_fixed_size: 0
    .kernarg_segment_align: 8
    .kernarg_segment_size: 16
    .language:       OpenCL C
    .language_version:
      - 2
      - 0
    .max_flat_workgroup_size: 256
    .name:           _Z13prep_x_kernelPKfP15HIP_vector_typeIjLj4EE
    .private_segment_fixed_size: 0
    .sgpr_count:     23
    .sgpr_spill_count: 0
    .symbol:         _Z13prep_x_kernelPKfP15HIP_vector_typeIjLj4EE.kd
    .uniform_work_group_size: 1
    .uses_dynamic_stack: false
    .vgpr_count:     36
    .vgpr_spill_count: 0
    .wavefront_size: 64
  - .agpr_count:     0
    .args:
      - .actual_access:  read_only
        .address_space:  global
        .offset:         0
        .size:           8
        .value_kind:     global_buffer
      - .actual_access:  write_only
        .address_space:  global
        .offset:         8
        .size:           8
        .value_kind:     global_buffer
      - .offset:         16
        .size:           4
        .value_kind:     by_value
      - .offset:         20
        .size:           4
        .value_kind:     by_value
      - .offset:         24
        .size:           4
        .value_kind:     by_value
      - .offset:         28
        .size:           4
        .value_kind:     by_value
    .group_segment_fixed_size: 0
    .kernarg_segment_align: 8
    .kernarg_segment_size: 32
    .language:       OpenCL C
    .language_version:
      - 2
      - 0
    .max_flat_workgroup_size: 256
    .name:           _Z13prep_w_kernelPKfP15HIP_vector_typeIjLj4EEiiii
    .private_segment_fixed_size: 0
    .sgpr_count:     15
    .sgpr_spill_count: 0
    .symbol:         _Z13prep_w_kernelPKfP15HIP_vector_typeIjLj4EEiiii.kd
    .uniform_work_group_size: 1
    .uses_dynamic_stack: false
    .vgpr_count:     34
    .vgpr_spill_count: 0
    .wavefront_size: 64
  - .agpr_count:     0
    .args:
      - .actual_access:  write_only
        .address_space:  global
        .offset:         0
        .size:           8
        .value_kind:     global_buffer
    .group_segment_fixed_size: 0
    .kernarg_segment_align: 8
    .kernarg_segment_size: 8
    .language:       OpenCL C
    .language_version:
      - 2
      - 0
    .max_flat_workgroup_size: 256
    .name:           _Z18zero_border_kernelP15HIP_vector_typeIjLj4EE
    .private_segment_fixed_size: 0
    .sgpr_count:     12
    .sgpr_spill_count: 0
    .symbol:         _Z18zero_border_kernelP15HIP_vector_typeIjLj4EE.kd
    .uniform_work_group_size: 1
    .uses_dynamic_stack: false
    .vgpr_count:     6
    .vgpr_spill_count: 0
    .wavefront_size: 64
  - .agpr_count:     0
    .args:
      - .actual_access:  read_only
        .address_space:  global
        .offset:         0
        .size:           8
        .value_kind:     global_buffer
      - .address_space:  global
        .offset:         8
        .size:           8
        .value_kind:     global_buffer
      - .actual_access:  read_only
        .address_space:  global
        .offset:         16
        .size:           8
        .value_kind:     global_buffer
      - .actual_access:  read_only
        .address_space:  global
        .offset:         24
        .size:           8
        .value_kind:     global_buffer
      - .actual_access:  read_only
        .address_space:  global
        .offset:         32
        .size:           8
        .value_kind:     global_buffer
      - .actual_access:  write_only
        .address_space:  global
        .offset:         40
        .size:           8
        .value_kind:     global_buffer
    .group_segment_fixed_size: 154880
    .kernarg_segment_align: 8
    .kernarg_segment_size: 48
    .language:       OpenCL C
    .language_version:
      - 2
      - 0
    .max_flat_workgroup_size: 512
    .name:           _Z12conv1_kernelPKfPK15HIP_vector_typeIjLj4EES0_S0_S0_PDF16_
    .private_segment_fixed_size: 0
    .sgpr_count:     46
    .sgpr_spill_count: 0
    .symbol:         _Z12conv1_kernelPKfPK15HIP_vector_typeIjLj4EES0_S0_S0_PDF16_.kd
    .uniform_work_group_size: 1
    .uses_dynamic_stack: false
    .vgpr_count:     256
    .vgpr_spill_count: 0
    .wavefront_size: 64
  - .agpr_count:     0
    .args:
      - .actual_access:  read_only
        .address_space:  global
        .offset:         0
        .size:           8
        .value_kind:     global_buffer
      - .actual_access:  read_only
        .address_space:  global
        .offset:         8
        .size:           8
        .value_kind:     global_buffer
      - .actual_access:  read_only
        .address_space:  global
        .offset:         16
        .size:           8
        .value_kind:     global_buffer
      - .actual_access:  write_only
        .address_space:  global
        .offset:         24
        .size:           8
        .value_kind:     global_buffer
      - .actual_access:  write_only
        .address_space:  global
        .offset:         32
        .size:           8
        .value_kind:     global_buffer
    .group_segment_fixed_size: 116480
    .kernarg_segment_align: 8
    .kernarg_segment_size: 40
    .language:       OpenCL C
    .language_version:
      - 2
      - 0
    .max_flat_workgroup_size: 512
    .name:           _Z12conv3_kernelPK15HIP_vector_typeIjLj4EES2_PKfPfS5_
    .private_segment_fixed_size: 0
    .sgpr_count:     22
    .sgpr_spill_count: 0
    .symbol:         _Z12conv3_kernelPK15HIP_vector_typeIjLj4EES2_PKfPfS5_.kd
    .uniform_work_group_size: 1
    .uses_dynamic_stack: false
    .vgpr_count:     128
    .vgpr_spill_count: 0
    .wavefront_size: 64
  - .agpr_count:     0
    .args:
      - .actual_access:  read_only
        .address_space:  global
        .offset:         0
        .size:           8
        .value_kind:     global_buffer
      - .actual_access:  read_only
        .address_space:  global
        .offset:         8
        .size:           8
        .value_kind:     global_buffer
      - .actual_access:  write_only
        .address_space:  global
        .offset:         16
        .size:           8
        .value_kind:     global_buffer
      - .address_space:  global
        .offset:         24
        .size:           8
        .value_kind:     global_buffer
    .group_segment_fixed_size: 32768
    .kernarg_segment_align: 8
    .kernarg_segment_size: 32
    .language:       OpenCL C
    .language_version:
      - 2
      - 0
    .max_flat_workgroup_size: 256
    .name:           _Z15nms_hist_kernelPKfS0_PjS1_
    .private_segment_fixed_size: 0
    .sgpr_count:     102
    .sgpr_spill_count: 0
    .symbol:         _Z15nms_hist_kernelPKfS0_PjS1_.kd
    .uniform_work_group_size: 1
    .uses_dynamic_stack: false
    .vgpr_count:     128
    .vgpr_spill_count: 0
    .wavefront_size: 64
  - .agpr_count:     0
    .args:
      - .actual_access:  read_only
        .address_space:  global
        .offset:         0
        .size:           8
        .value_kind:     global_buffer
      - .actual_access:  write_only
        .address_space:  global
        .offset:         8
        .size:           8
        .value_kind:     global_buffer
    .group_segment_fixed_size: 4096
    .kernarg_segment_align: 8
    .kernarg_segment_size: 16
    .language:       OpenCL C
    .language_version:
      - 2
      - 0
    .max_flat_workgroup_size: 1024
    .name:           _Z17select_bin_kernelPKjPi
    .private_segment_fixed_size: 0
    .sgpr_count:     23
    .sgpr_spill_count: 0
    .symbol:         _Z17select_bin_kernelPKjPi.kd
    .uniform_work_group_size: 1
    .uses_dynamic_stack: false
    .vgpr_count:     13
    .vgpr_spill_count: 0
    .wavefront_size: 64
  - .agpr_count:     0
    .args:
      - .actual_access:  read_only
        .address_space:  global
        .offset:         0
        .size:           8
        .value_kind:     global_buffer
      - .actual_access:  read_only
        .address_space:  global
        .offset:         8
        .size:           8
        .value_kind:     global_buffer
      - .address_space:  global
        .offset:         16
        .size:           8
        .value_kind:     global_buffer
      - .actual_access:  write_only
        .address_space:  global
        .offset:         24
        .size:           8
        .value_kind:     global_buffer
    .group_segment_fixed_size: 2052
    .kernarg_segment_align: 8
    .kernarg_segment_size: 32
    .language:       OpenCL C
    .language_version:
      - 2
      - 0
    .max_flat_workgroup_size: 512
    .name:           _Z14collect_kernelPKjS0_PiS1_
    .private_segment_fixed_size: 0
    .sgpr_count:     70
    .sgpr_spill_count: 0
    .symbol:         _Z14collect_kernelPKjS0_PiS1_.kd
    .uniform_work_group_size: 1
    .uses_dynamic_stack: false
    .vgpr_count:     34
    .vgpr_spill_count: 0
    .wavefront_size: 64
  - .agpr_count:     0
    .args:
      - .actual_access:  read_only
        .address_space:  global
        .offset:         0
        .size:           8
        .value_kind:     global_buffer
      - .actual_access:  read_only
        .address_space:  global
        .offset:         8
        .size:           8
        .value_kind:     global_buffer
      - .actual_access:  read_only
        .address_space:  global
        .offset:         16
        .size:           8
        .value_kind:     global_buffer
      - .actual_access:  read_only
        .address_space:  global
        .offset:         24
        .size:           8
        .value_kind:     global_buffer
      - .actual_access:  write_only
        .address_space:  global
        .offset:         32
        .size:           8
        .value_kind:     global_buffer
    .group_segment_fixed_size: 49664
    .kernarg_segment_align: 8
    .kernarg_segment_size: 40
    .language:       OpenCL C
    .language_version:
      - 2
      - 0
    .max_flat_workgroup_size: 1024
    .name:           _Z11rank_kernelPKfS0_PKiS2_Pi
    .private_segment_fixed_size: 0
    .sgpr_count:     23
    .sgpr_spill_count: 0
    .symbol:         _Z11rank_kernelPKfS0_PKiS2_Pi.kd
    .uniform_work_group_size: 1
    .uses_dynamic_stack: false
    .vgpr_count:     12
    .vgpr_spill_count: 0
    .wavefront_size: 64
  - .agpr_count:     0
    .args:
      - .actual_access:  read_only
        .address_space:  global
        .offset:         0
        .size:           8
        .value_kind:     global_buffer
      - .actual_access:  read_only
        .address_space:  global
        .offset:         8
        .size:           8
        .value_kind:     global_buffer
      - .actual_access:  write_only
        .address_space:  global
        .offset:         16
        .size:           8
        .value_kind:     global_buffer
      - .actual_access:  write_only
        .address_space:  global
        .offset:         24
        .size:           8
        .value_kind:     global_buffer
    .group_segment_fixed_size: 0
    .kernarg_segment_align: 8
    .kernarg_segment_size: 32
    .language:       OpenCL C
    .language_version:
      - 2
      - 0
    .max_flat_workgroup_size: 256
    .name:           _Z15prep_kvw_kernelPKfS0_PDF16_S1_
    .private_segment_fixed_size: 0
    .sgpr_count:     14
    .sgpr_spill_count: 0
    .symbol:         _Z15prep_kvw_kernelPKfS0_PDF16_S1_.kd
    .uniform_work_group_size: 1
    .uses_dynamic_stack: false
    .vgpr_count:     7
    .vgpr_spill_count: 0
    .wavefront_size: 64
  - .agpr_count:     0
    .args:
      - .actual_access:  read_only
        .address_space:  global
        .offset:         0
        .size:           8
        .value_kind:     global_buffer
      - .actual_access:  read_only
        .address_space:  global
        .offset:         8
        .size:           8
        .value_kind:     global_buffer
      - .actual_access:  read_only
        .address_space:  global
        .offset:         16
        .size:           8
        .value_kind:     global_buffer
      - .actual_access:  read_only
        .address_space:  global
        .offset:         24
        .size:           8
        .value_kind:     global_buffer
      - .actual_access:  write_only
        .address_space:  global
        .offset:         32
        .size:           8
        .value_kind:     global_buffer
    .group_segment_fixed_size: 67856
    .kernarg_segment_align: 8
    .kernarg_segment_size: 40
    .language:       OpenCL C
    .language_version:
      - 2
      - 0
    .max_flat_workgroup_size: 448
    .name:           _Z17cross_attn_kernelPKDF16_S0_S0_S0_Pf
    .private_segment_fixed_size: 0
    .sgpr_count:     26
    .sgpr_spill_count: 0
    .symbol:         _Z17cross_attn_kernelPKDF16_S0_S0_S0_Pf.kd
    .uniform_work_group_size: 1
    .uses_dynamic_stack: false
    .vgpr_count:     74
    .vgpr_spill_count: 0
    .wavefront_size: 64
  - .agpr_count:     0
    .args:
      - .offset:         0
        .size:           424
        .value_kind:     by_value
      - .offset:         424
        .size:           88
        .value_kind:     by_value
    .group_segment_fixed_size: 137216
    .kernarg_segment_align: 8
    .kernarg_segment_size: 512
    .language:       OpenCL C
    .language_version:
      - 2
      - 0
    .max_flat_workgroup_size: 512
    .name:           _Z12tailA_kernel5TailP3KvP
    .private_segment_fixed_size: 0
    .sgpr_count:     44
    .sgpr_spill_count: 0
    .symbol:         _Z12tailA_kernel5TailP3KvP.kd
    .uniform_work_group_size: 1
    .uses_dynamic_stack: false
    .vgpr_count:     200
    .vgpr_spill_count: 0
    .wavefront_size: 64
  - .agpr_count:     0
    .args:
      - .offset:         0
        .size:           424
        .value_kind:     by_value
      - .offset:         424
        .size:           88
        .value_kind:     by_value
    .group_segment_fixed_size: 146592
    .kernarg_segment_align: 8
    .kernarg_segment_size: 512
    .language:       OpenCL C
    .language_version:
      - 2
      - 0
    .max_flat_workgroup_size: 512
    .name:           _Z12tailB_kernel5TailP3KvP
    .private_segment_fixed_size: 0
    .sgpr_count:     44
    .sgpr_spill_count: 0
    .symbol:         _Z12tailB_kernel5TailP3KvP.kd
    .uniform_work_group_size: 1
    .uses_dynamic_stack: false
    .vgpr_count:     216
    .vgpr_spill_count: 0
    .wavefront_size: 64
  - .agpr_count:     0
    .args:
      - .offset:         0
        .size:           424
        .value_kind:     by_value
    .group_segment_fixed_size: 36896
    .kernarg_segment_align: 8
    .kernarg_segment_size: 424
    .language:       OpenCL C
    .language_version:
      - 2
      - 0
    .max_flat_workgroup_size: 512
    .name:           _Z12tailC_kernel5TailP
    .private_segment_fixed_size: 0
    .sgpr_count:     58
    .sgpr_spill_count: 0
    .symbol:         _Z12tailC_kernel5TailP.kd
    .uniform_work_group_size: 1
    .uses_dynamic_stack: false
    .vgpr_count:     113
    .vgpr_spill_count: 0
    .wavefront_size: 64
  - .agpr_count:     0
    .args:
      - .offset:         0
        .size:           344
        .value_kind:     by_value
    .group_segment_fixed_size: 0
    .kernarg_segment_align: 8
    .kernarg_segment_size: 344
    .language:       OpenCL C
    .language_version:
      - 2
      - 0
    .max_flat_workgroup_size: 256
    .name:           _Z15prep_all_kernel5PrepP
    .private_segment_fixed_size: 0
    .sgpr_count:     31
    .sgpr_spill_count: 0
    .symbol:         _Z15prep_all_kernel5PrepP.kd
    .uniform_work_group_size: 1
    .uses_dynamic_stack: false
    .vgpr_count:     39
    .vgpr_spill_count: 0
    .wavefront_size: 64
  - .agpr_count:     0
    .args:
      - .actual_access:  read_only
        .address_space:  global
        .offset:         0
        .size:           8
        .value_kind:     global_buffer
      - .actual_access:  read_only
        .address_space:  global
        .offset:         8
        .size:           8
        .value_kind:     global_buffer
      - .actual_access:  read_only
        .address_space:  global
        .offset:         16
        .size:           8
        .value_kind:     global_buffer
      - .actual_access:  read_only
        .address_space:  global
        .offset:         24
        .size:           8
        .value_kind:     global_buffer
      - .actual_access:  read_only
        .address_space:  global
        .offset:         32
        .size:           8
        .value_kind:     global_buffer
      - .actual_access:  write_only
        .address_space:  global
        .offset:         40
        .size:           8
        .value_kind:     global_buffer
      - .actual_access:  read_only
        .address_space:  global
        .offset:         48
        .size:           8
        .value_kind:     global_buffer
      - .actual_access:  read_only
        .address_space:  global
        .offset:         56
        .size:           8
        .value_kind:     global_buffer
    .group_segment_fixed_size: 130304
    .kernarg_segment_align: 8
    .kernarg_segment_size: 64
    .language:       OpenCL C
    .language_version:
      - 2
      - 0
    .max_flat_workgroup_size: 512
    .name:           _Z11conv_kernelILi8ELi128ELi0EEvPK15HIP_vector_typeIjLj4EES3_PKfS5_S5_PDF16_PfS7_
    .private_segment_fixed_size: 0
    .sgpr_count:     30
    .sgpr_spill_count: 0
    .symbol:         _Z11conv_kernelILi8ELi128ELi0EEvPK15HIP_vector_typeIjLj4EES3_PKfS5_S5_PDF16_PfS7_.kd
    .uniform_work_group_size: 1
    .uses_dynamic_stack: false
    .vgpr_count:     254
    .vgpr_spill_count: 0
    .wavefront_size: 64
